# static s_setprio 1 for waves 0-3 (older half) at the start of the stick-breaking attention items
# speedup vs baseline: 1.0046x; 1.0008x over previous
.LBB0_586:
	s_and_b64 vcc, exec, s[10:11]
	s_cbranch_vccz .LBB0_496
	s_and_b64 vcc, exec, s[82:83]
	s_cbranch_vccz .Lprio_skip_0
	s_setprio 1

.LBB0_1977:
	s_and_b64 vcc, exec, s[6:7]
	s_cbranch_vccz .LBB0_1887
	s_and_b64 vcc, exec, s[74:75]
	s_cbranch_vccz .Lprio_skip_1
	s_setprio 1
